# c10
# speedup vs baseline: 1.0325x; 1.0013x over previous
.LBB1_2:
	s_load_dwordx4 s[0:3], s[0:1], 0x10
	v_lshrrev_b32_e32 v70, 5, v1
	v_and_b32_e32 v71, 31, v0
	v_lshlrev_b32_e32 v0, 8, v70
	s_lshl_b32 s36, s21, 7
	s_lshl_b32 s8, s15, 5
	v_add_u32_e32 v1, s36, v0
	s_and_b32 s35, s8, 0x60
	s_waitcnt vmcnt(6)
	v_or_b32_e32 v1, v1, v71
	v_or3_b32 v3, v0, s35, v71
	v_lshlrev_b32_e32 v0, 7, v70
	s_addk_i32 s22, 0x4000
	s_addk_i32 s25, 0x4000
	s_addk_i32 s27, 0x4000
	v_or3_b32 v0, s35, v0, v71
	v_lshlrev_b32_e32 v8, 4, v1
	s_barrier
	s_barrier
	s_add_u32 s10, s23, s26
	s_addc_u32 s11, s24, 0
	s_add_i32 s49, s28, 0
	s_add_i32 s49, s49, 0x1e000
	s_add_i32 s8, 0, 0x14000
	s_add_u32 s4, s4, s13
	s_addc_u32 s5, s5, 0
	v_lshl_add_u64 v[4:5], s[4:5], 0, v[4:5]
	s_mov_b64 s[4:5], 0x12000
	s_add_i32 s20, s20, s18
	s_mulk_i32 s19, 0xc00
	s_add_i32 s17, s17, s18
	s_mulk_i32 s16, 0xc00
	v_lshl_add_u32 v72, v0, 1, 0
	v_lshl_add_u64 v[0:1], s[10:11], 0, v[6:7]
	v_lshl_add_u64 v[68:69], v[4:5], 0, s[4:5]
	s_sub_i32 s4, s20, s19
	s_sub_i32 s10, s17, s16
	s_add_i32 s14, s14, s18
	s_mulk_i32 s12, 0xc00
	v_mad_u32_u24 v9, v3, 24, 0
	v_mad_u32_u24 v3, v3, 24, s8
	s_addk_i32 s4, 0x4000
	s_addk_i32 s10, 0x2000
	s_sub_i32 s12, s14, s12
	s_mov_b32 s14, 0xffff6000
	s_movk_i32 s16, 0x8000
	s_add_i32 s52, s8, s22
	s_add_i32 s54, s8, s27
	s_movk_i32 s20, 0xa000
	s_movk_i32 s22, 0xc000
	s_movk_i32 s26, 0xe000
	v_add_u32_e32 v78, 0x4000, v9
	v_add_u32_e32 v75, 0xe000, v9
	v_add_u32_e32 v82, 0x4000, v3
	v_add_u32_e32 v81, 0x4c00, v9
	v_add_u32_e32 v80, 0x7000, v9
	v_add_u32_e32 v79, 0x7c00, v9
	v_add_u32_e32 v76, 0xec00, v9
	v_add_u32_e32 v74, 0x11000, v9
	v_add_u32_e32 v73, 0x11c00, v9
	v_add_u32_e32 v83, 0x4c00, v3
	v_add_u32_e32 v84, 0x7000, v3
	v_add_u32_e32 v85, 0x7c00, v3
	s_ashr_i32 s5, s4, 31
	s_ashr_i32 s11, s10, 31
	s_ashr_i32 s13, s12, 31
	v_add_u32_e32 v77, 0, v8
	s_mov_b32 s15, -1
	s_add_i32 s50, s8, s18
	s_mov_b32 s17, -1
	s_add_i32 s51, s38, 0x16000
	s_mov_b64 s[18:19], 0x18000
	s_add_i32 s53, s8, s25
	s_mov_b32 s21, -1
	s_mov_b32 s23, -1
	s_mov_b64 s[24:25], 0x24000
	v_add_u32_e32 v86, s8, v8
	s_mov_b32 s27, -1
	s_mov_b64 s[28:29], 0x30000
	s_mov_b32 s55, 0
	v_mov_b32_e32 v3, v2
	v_mov_b32_e32 v4, v2
	v_mov_b32_e32 v5, v2
	v_mov_b32_e32 v6, v2
	v_mov_b32_e32 v7, v2
	v_mov_b32_e32 v8, v2
	v_mov_b32_e32 v9, v2
	v_mov_b32_e32 v10, v2
	v_mov_b32_e32 v11, v2
	v_mov_b32_e32 v12, v2
	v_mov_b32_e32 v13, v2
	v_mov_b32_e32 v14, v2
	v_mov_b32_e32 v15, v2
	v_mov_b32_e32 v16, v2
	v_mov_b32_e32 v17, v2
	v_mov_b32_e32 v18, v2
	v_mov_b32_e32 v19, v2
	v_mov_b32_e32 v20, v2
	v_mov_b32_e32 v21, v2
	v_mov_b32_e32 v22, v2
	v_mov_b32_e32 v23, v2
	v_mov_b32_e32 v24, v2
	v_mov_b32_e32 v25, v2
	v_mov_b32_e32 v26, v2
	v_mov_b32_e32 v27, v2
	v_mov_b32_e32 v28, v2
	v_mov_b32_e32 v29, v2
	v_mov_b32_e32 v30, v2
	v_mov_b32_e32 v31, v2
	v_mov_b32_e32 v32, v2
	v_mov_b32_e32 v33, v2
	v_mov_b32_e32 v34, v2
	v_mov_b32_e32 v35, v2
	v_mov_b32_e32 v36, v2
	v_mov_b32_e32 v37, v2
	v_mov_b32_e32 v38, v2
	v_mov_b32_e32 v39, v2
	v_mov_b32_e32 v40, v2
	v_mov_b32_e32 v41, v2
	v_mov_b32_e32 v42, v2
	v_mov_b32_e32 v43, v2
	v_mov_b32_e32 v44, v2
	v_mov_b32_e32 v45, v2
	v_mov_b32_e32 v46, v2
	v_mov_b32_e32 v47, v2
	v_mov_b32_e32 v48, v2
	v_mov_b32_e32 v49, v2
	v_mov_b32_e32 v50, v2
	v_mov_b32_e32 v51, v2
	v_mov_b32_e32 v52, v2
	v_mov_b32_e32 v53, v2
	v_mov_b32_e32 v54, v2
	v_mov_b32_e32 v55, v2
	v_mov_b32_e32 v56, v2
	v_mov_b32_e32 v57, v2
	v_mov_b32_e32 v58, v2
	v_mov_b32_e32 v59, v2
	v_mov_b32_e32 v60, v2
	v_mov_b32_e32 v61, v2
	v_mov_b32_e32 v62, v2
	v_mov_b32_e32 v63, v2
	v_mov_b32_e32 v64, v2
	v_mov_b32_e32 v65, v2
	v_add_u32_e32 v87, 0x1e000, v72
	v_mov_b32_e32 v88, 0x7f7f7f7f
	v_readfirstlane_b32 s72, v68
	v_readfirstlane_b32 s73, v69
	v_readfirstlane_b32 s76, v66
	v_readfirstlane_b32 s77, v67
	v_readfirstlane_b32 s80, v0
	v_readfirstlane_b32 s81, v1
	s_nop 3
	v_subrev_u32_e32 v160, s80, v0
	s_sub_u32 s72, s72, 0xa000
	s_subb_u32 s73, s73, 0
	s_add_u32 s76, s76, 0x18000
	s_addc_u32 s77, s77, 0
	v_lshlrev_b32_e32 v161, 2, v160
	v_add_u32_e32 v162, 0x2000, v161
	v_add_u32_e32 v163, 0x4000, v161
	v_add_u32_e32 v164, 0x6000, v161
	v_add_u32_e32 v165, 0x8000, v161
	v_add_u32_e32 v166, 0xa000, v161
	v_add_u32_e32 v167, s12, v161
	v_add_u32_e32 v168, s10, v161
	v_add_u32_e32 v169, s4, v161
	v_add_u32_e32 v170, 0xc000, v167
	v_add_u32_e32 v171, 0xc000, v168
	v_add_u32_e32 v172, 0xc000, v169
	v_add_u32_e32 v173, 0x18000, v167
	v_add_u32_e32 v174, 0x18000, v168
	v_add_u32_e32 v175, 0x18000, v169
.LBB1_3:
	s_and_b32 s8, s55, 6
	ds_read_b128 v[114:117], v77
	ds_read_b128 v[118:121], v77 offset:512
	ds_read_b128 v[122:125], v77 offset:1024
	ds_read_b128 v[126:129], v77 offset:1536
	ds_read_b64 v[90:91], v78
	ds_read_b64 v[92:93], v78 offset:8
	ds_read_b64 v[94:95], v78 offset:16
	ds_read_b64 v[96:97], v81
	ds_read_b64 v[98:99], v81 offset:8
	ds_read_b64 v[100:101], v81 offset:16
	v_lshl_add_u32 v89, s8, 9, v87
	ds_read_u16 v154, v89
	ds_read_b128 v[130:133], v77 offset:8192
	ds_read_b128 v[134:137], v77 offset:8704
	ds_read_b128 v[138:141], v77 offset:9216
	ds_read_b128 v[142:145], v77 offset:9728
	ds_read_b64 v[102:103], v80
	ds_read_b64 v[104:105], v80 offset:8
	ds_read_b64 v[106:107], v80 offset:16
	s_mov_b32 m0, s50
	ds_read_b64 v[108:109], v79
	ds_read_b64 v[110:111], v79 offset:8
	ds_read_b64 v[112:113], v79 offset:16
	ds_read_u16 v89, v89 offset:512
	global_load_lds_dwordx4 v161, s[72:73]
	s_mov_b32 m0, s51
	s_add_i32 s56, s37, s55
	global_load_lds_dwordx4 v162, s[72:73]
	s_mov_b32 m0, s52
	s_add_i32 s8, s56, 4
	global_load_lds_dwordx4 v167, s[76:77]
	s_mov_b32 m0, s53
	s_min_u32 s57, s8, 63
	global_load_lds_dwordx4 v168, s[76:77]
	s_mov_b32 m0, s54
	s_lshl_b32 s8, s57, 10
	global_load_lds_dwordx4 v169, s[76:77]
	s_add_u32 s82, s80, s8
	s_addc_u32 s83, s81, 0
	s_lshl_b32 s8, s57, 9
	s_and_b32 s8, s8, 0xe00
	s_add_i32 m0, s49, s8
	s_add_i32 s57, s55, 4
	global_load_lds_dword v160, s[82:83]
	s_waitcnt vmcnt(6)
	s_waitcnt lgkmcnt(0)
	s_barrier
	s_setprio 1
	s_waitcnt lgkmcnt(0)
	v_mfma_scale_f32_32x32x64_f8f6f4 v[50:65], v[90:95], v[114:117], v[50:65], v154, v88 op_sel_hi:[0,0,0] cbsz:2 blgp:4
	v_mfma_scale_f32_32x32x64_f8f6f4 v[34:49], v[90:95], v[118:121], v[34:49], v154, v88 op_sel_hi:[0,0,0] cbsz:2 blgp:4
	v_mfma_scale_f32_32x32x64_f8f6f4 v[18:33], v[90:95], v[122:125], v[18:33], v154, v88 op_sel_hi:[0,0,0] cbsz:2 blgp:4
	v_mfma_scale_f32_32x32x64_f8f6f4 v[2:17], v[90:95], v[126:129], v[2:17], v154, v88 op_sel_hi:[0,0,0] cbsz:2 blgp:4
	v_mfma_scale_f32_32x32x64_f8f6f4 v[50:65], v[96:101], v[114:117], v[50:65], v154, v88 op_sel:[1,0,0] op_sel_hi:[0,0,0] cbsz:2 blgp:4
	v_mfma_scale_f32_32x32x64_f8f6f4 v[34:49], v[96:101], v[118:121], v[34:49], v154, v88 op_sel:[1,0,0] op_sel_hi:[0,0,0] cbsz:2 blgp:4
	v_mfma_scale_f32_32x32x64_f8f6f4 v[18:33], v[96:101], v[122:125], v[18:33], v154, v88 op_sel:[1,0,0] op_sel_hi:[0,0,0] cbsz:2 blgp:4
	v_mfma_scale_f32_32x32x64_f8f6f4 v[2:17], v[96:101], v[126:129], v[2:17], v154, v88 op_sel:[1,0,0] op_sel_hi:[0,0,0] cbsz:2 blgp:4
	v_mfma_scale_f32_32x32x64_f8f6f4 v[50:65], v[102:107], v[130:133], v[50:65], v89, v88 op_sel_hi:[0,0,0] cbsz:2 blgp:4
	v_mfma_scale_f32_32x32x64_f8f6f4 v[34:49], v[102:107], v[134:137], v[34:49], v89, v88 op_sel_hi:[0,0,0] cbsz:2 blgp:4
	v_mfma_scale_f32_32x32x64_f8f6f4 v[18:33], v[102:107], v[138:141], v[18:33], v89, v88 op_sel_hi:[0,0,0] cbsz:2 blgp:4
	v_mfma_scale_f32_32x32x64_f8f6f4 v[2:17], v[102:107], v[142:145], v[2:17], v89, v88 op_sel_hi:[0,0,0] cbsz:2 blgp:4
	v_mfma_scale_f32_32x32x64_f8f6f4 v[50:65], v[108:113], v[130:133], v[50:65], v89, v88 op_sel:[1,0,0] op_sel_hi:[0,0,0] cbsz:2 blgp:4
	v_mfma_scale_f32_32x32x64_f8f6f4 v[34:49], v[108:113], v[134:137], v[34:49], v89, v88 op_sel:[1,0,0] op_sel_hi:[0,0,0] cbsz:2 blgp:4
	v_mfma_scale_f32_32x32x64_f8f6f4 v[18:33], v[108:113], v[138:141], v[18:33], v89, v88 op_sel:[1,0,0] op_sel_hi:[0,0,0] cbsz:2 blgp:4
	v_mfma_scale_f32_32x32x64_f8f6f4 v[2:17], v[108:113], v[142:145], v[2:17], v89, v88 op_sel:[1,0,0] op_sel_hi:[0,0,0] cbsz:2 blgp:4
	s_setprio 0
	s_barrier
	s_add_i32 s8, s55, 2
	s_and_b32 s8, s8, 6
	ds_read_b128 v[114:117], v77 offset:40960
	ds_read_b128 v[118:121], v77 offset:41472
	ds_read_b128 v[122:125], v77 offset:41984
	ds_read_b128 v[126:129], v77 offset:42496
	ds_read_b64 v[90:91], v75
	ds_read_b64 v[92:93], v75 offset:8
	ds_read_b64 v[94:95], v75 offset:16
	ds_read_b64 v[96:97], v76
	ds_read_b64 v[98:99], v76 offset:8
	ds_read_b64 v[100:101], v76 offset:16
	v_lshl_add_u32 v89, s8, 9, v87
	ds_read_u16 v154, v89
	ds_read_b128 v[130:133], v77 offset:49152
	ds_read_b128 v[134:137], v77 offset:49664
	ds_read_b128 v[138:141], v77 offset:50176
	ds_read_b128 v[142:145], v77 offset:50688
	ds_read_b64 v[102:103], v74
	ds_read_b64 v[104:105], v74 offset:8
	ds_read_b64 v[106:107], v74 offset:16
	s_mov_b32 m0, s38
	ds_read_b64 v[108:109], v73
	ds_read_b64 v[110:111], v73 offset:8
	ds_read_b64 v[112:113], v73 offset:16
	ds_read_u16 v89, v89 offset:512
	global_load_lds_dwordx4 v163, s[72:73]
	s_mov_b32 m0, s39
	s_add_i32 s8, s56, 6
	global_load_lds_dwordx4 v164, s[72:73]
	s_mov_b32 m0, s40
	s_min_u32 s58, s8, 63
	global_load_lds_dwordx4 v170, s[76:77]
	s_mov_b32 m0, s41
	s_lshl_b32 s8, s58, 10
	global_load_lds_dwordx4 v171, s[76:77]
	s_mov_b32 m0, s42
	s_nop 0
	global_load_lds_dwordx4 v172, s[76:77]
	s_add_u32 s82, s80, s8
	s_addc_u32 s83, s81, 0
	s_lshl_b32 s8, s58, 9
	s_and_b32 s8, s8, 0xe00
	s_add_i32 m0, s49, s8
	s_nop 0
	global_load_lds_dword v160, s[82:83]
	s_waitcnt vmcnt(6)
	s_waitcnt lgkmcnt(0)
	s_barrier
	s_setprio 1
	s_waitcnt lgkmcnt(0)
	v_mfma_scale_f32_32x32x64_f8f6f4 v[50:65], v[90:95], v[114:117], v[50:65], v154, v88 op_sel_hi:[0,0,0] cbsz:2 blgp:4
	v_mfma_scale_f32_32x32x64_f8f6f4 v[34:49], v[90:95], v[118:121], v[34:49], v154, v88 op_sel_hi:[0,0,0] cbsz:2 blgp:4
	v_mfma_scale_f32_32x32x64_f8f6f4 v[18:33], v[90:95], v[122:125], v[18:33], v154, v88 op_sel_hi:[0,0,0] cbsz:2 blgp:4
	v_mfma_scale_f32_32x32x64_f8f6f4 v[2:17], v[90:95], v[126:129], v[2:17], v154, v88 op_sel_hi:[0,0,0] cbsz:2 blgp:4
	v_mfma_scale_f32_32x32x64_f8f6f4 v[50:65], v[96:101], v[114:117], v[50:65], v154, v88 op_sel:[1,0,0] op_sel_hi:[0,0,0] cbsz:2 blgp:4
	v_mfma_scale_f32_32x32x64_f8f6f4 v[34:49], v[96:101], v[118:121], v[34:49], v154, v88 op_sel:[1,0,0] op_sel_hi:[0,0,0] cbsz:2 blgp:4
	v_mfma_scale_f32_32x32x64_f8f6f4 v[18:33], v[96:101], v[122:125], v[18:33], v154, v88 op_sel:[1,0,0] op_sel_hi:[0,0,0] cbsz:2 blgp:4
	v_mfma_scale_f32_32x32x64_f8f6f4 v[2:17], v[96:101], v[126:129], v[2:17], v154, v88 op_sel:[1,0,0] op_sel_hi:[0,0,0] cbsz:2 blgp:4
	v_mfma_scale_f32_32x32x64_f8f6f4 v[50:65], v[102:107], v[130:133], v[50:65], v89, v88 op_sel_hi:[0,0,0] cbsz:2 blgp:4
	v_mfma_scale_f32_32x32x64_f8f6f4 v[34:49], v[102:107], v[134:137], v[34:49], v89, v88 op_sel_hi:[0,0,0] cbsz:2 blgp:4
	v_mfma_scale_f32_32x32x64_f8f6f4 v[18:33], v[102:107], v[138:141], v[18:33], v89, v88 op_sel_hi:[0,0,0] cbsz:2 blgp:4
	v_mfma_scale_f32_32x32x64_f8f6f4 v[2:17], v[102:107], v[142:145], v[2:17], v89, v88 op_sel_hi:[0,0,0] cbsz:2 blgp:4
	v_mfma_scale_f32_32x32x64_f8f6f4 v[50:65], v[108:113], v[130:133], v[50:65], v89, v88 op_sel:[1,0,0] op_sel_hi:[0,0,0] cbsz:2 blgp:4
	v_mfma_scale_f32_32x32x64_f8f6f4 v[34:49], v[108:113], v[134:137], v[34:49], v89, v88 op_sel:[1,0,0] op_sel_hi:[0,0,0] cbsz:2 blgp:4
	v_mfma_scale_f32_32x32x64_f8f6f4 v[18:33], v[108:113], v[138:141], v[18:33], v89, v88 op_sel:[1,0,0] op_sel_hi:[0,0,0] cbsz:2 blgp:4
	v_mfma_scale_f32_32x32x64_f8f6f4 v[2:17], v[108:113], v[142:145], v[2:17], v89, v88 op_sel:[1,0,0] op_sel_hi:[0,0,0] cbsz:2 blgp:4
	s_setprio 0
	s_barrier
	s_and_b32 s8, s57, 6
	ds_read_b128 v[114:117], v86
	ds_read_b128 v[118:121], v86 offset:512
	ds_read_b128 v[122:125], v86 offset:1024
	ds_read_b128 v[126:129], v86 offset:1536
	ds_read_b64 v[90:91], v82
	ds_read_b64 v[92:93], v82 offset:8
	ds_read_b64 v[94:95], v82 offset:16
	ds_read_b64 v[96:97], v83
	ds_read_b64 v[98:99], v83 offset:8
	ds_read_b64 v[100:101], v83 offset:16
	v_lshl_add_u32 v89, s8, 9, v87
	ds_read_u16 v154, v89
	ds_read_b128 v[130:133], v86 offset:8192
	ds_read_b128 v[134:137], v86 offset:8704
	ds_read_b128 v[138:141], v86 offset:9216
	ds_read_b128 v[142:145], v86 offset:9728
	ds_read_b64 v[102:103], v84
	ds_read_b64 v[104:105], v84 offset:8
	ds_read_b64 v[106:107], v84 offset:16
	s_mov_b32 m0, s43
	ds_read_b64 v[108:109], v85
	ds_read_b64 v[110:111], v85 offset:8
	ds_read_b64 v[112:113], v85 offset:16
	ds_read_u16 v89, v89 offset:512
	global_load_lds_dwordx4 v165, s[72:73]
	s_mov_b32 m0, s44
	s_nop 0
	global_load_lds_dwordx4 v166, s[72:73]
	s_mov_b32 m0, s45
	s_add_i32 s56, s56, 8
	global_load_lds_dwordx4 v173, s[76:77]
	s_mov_b32 m0, s46
	s_min_u32 s56, s56, 63
	global_load_lds_dwordx4 v174, s[76:77]
	s_mov_b32 m0, s47
	s_lshl_b32 s8, s56, 10
	global_load_lds_dwordx4 v175, s[76:77]
	s_add_u32 s82, s80, s8
	s_addc_u32 s83, s81, 0
	s_lshl_b32 s8, s56, 9
	s_and_b32 s8, s8, 0xe00
	s_add_i32 m0, s49, s8
	s_nop 0
	global_load_lds_dword v160, s[82:83]
	s_waitcnt vmcnt(6)
	s_waitcnt lgkmcnt(0)
	s_barrier
	s_setprio 1
	s_waitcnt lgkmcnt(0)
	v_mfma_scale_f32_32x32x64_f8f6f4 v[50:65], v[90:95], v[114:117], v[50:65], v154, v88 op_sel_hi:[0,0,0] cbsz:2 blgp:4
	v_mfma_scale_f32_32x32x64_f8f6f4 v[34:49], v[90:95], v[118:121], v[34:49], v154, v88 op_sel_hi:[0,0,0] cbsz:2 blgp:4
	v_mfma_scale_f32_32x32x64_f8f6f4 v[18:33], v[90:95], v[122:125], v[18:33], v154, v88 op_sel_hi:[0,0,0] cbsz:2 blgp:4
	v_mfma_scale_f32_32x32x64_f8f6f4 v[2:17], v[90:95], v[126:129], v[2:17], v154, v88 op_sel_hi:[0,0,0] cbsz:2 blgp:4
	v_mfma_scale_f32_32x32x64_f8f6f4 v[50:65], v[96:101], v[114:117], v[50:65], v154, v88 op_sel:[1,0,0] op_sel_hi:[0,0,0] cbsz:2 blgp:4
	v_mfma_scale_f32_32x32x64_f8f6f4 v[34:49], v[96:101], v[118:121], v[34:49], v154, v88 op_sel:[1,0,0] op_sel_hi:[0,0,0] cbsz:2 blgp:4
	v_mfma_scale_f32_32x32x64_f8f6f4 v[18:33], v[96:101], v[122:125], v[18:33], v154, v88 op_sel:[1,0,0] op_sel_hi:[0,0,0] cbsz:2 blgp:4
	v_mfma_scale_f32_32x32x64_f8f6f4 v[2:17], v[96:101], v[126:129], v[2:17], v154, v88 op_sel:[1,0,0] op_sel_hi:[0,0,0] cbsz:2 blgp:4
	v_mfma_scale_f32_32x32x64_f8f6f4 v[50:65], v[102:107], v[130:133], v[50:65], v89, v88 op_sel_hi:[0,0,0] cbsz:2 blgp:4
	v_mfma_scale_f32_32x32x64_f8f6f4 v[34:49], v[102:107], v[134:137], v[34:49], v89, v88 op_sel_hi:[0,0,0] cbsz:2 blgp:4
	v_mfma_scale_f32_32x32x64_f8f6f4 v[18:33], v[102:107], v[138:141], v[18:33], v89, v88 op_sel_hi:[0,0,0] cbsz:2 blgp:4
	v_mfma_scale_f32_32x32x64_f8f6f4 v[2:17], v[102:107], v[142:145], v[2:17], v89, v88 op_sel_hi:[0,0,0] cbsz:2 blgp:4
	v_mfma_scale_f32_32x32x64_f8f6f4 v[50:65], v[108:113], v[130:133], v[50:65], v89, v88 op_sel:[1,0,0] op_sel_hi:[0,0,0] cbsz:2 blgp:4
	v_mfma_scale_f32_32x32x64_f8f6f4 v[34:49], v[108:113], v[134:137], v[34:49], v89, v88 op_sel:[1,0,0] op_sel_hi:[0,0,0] cbsz:2 blgp:4
	v_mfma_scale_f32_32x32x64_f8f6f4 v[18:33], v[108:113], v[138:141], v[18:33], v89, v88 op_sel:[1,0,0] op_sel_hi:[0,0,0] cbsz:2 blgp:4
	v_mfma_scale_f32_32x32x64_f8f6f4 v[2:17], v[108:113], v[142:145], v[2:17], v89, v88 op_sel:[1,0,0] op_sel_hi:[0,0,0] cbsz:2 blgp:4
	s_setprio 0
	s_barrier
	s_add_i32 s48, s48, 3
	s_add_i32 s55, s55, 6
	s_add_u32 s72, s72, 0xc000
	s_addc_u32 s73, s73, 0
	s_add_u32 s76, s76, 0x24000
	s_addc_u32 s77, s77, 0
	s_cmp_lt_u32 s48, 27
	s_cbranch_scc1 .LBB1_3
	ds_read_b128 v[66:69], v77
	ds_read_b128 v[106:109], v77 offset:512
	ds_read_b128 v[110:113], v77 offset:1024
	ds_read_b128 v[114:117], v77 offset:1536
	ds_read_b64 v[82:83], v78
	ds_read_b64 v[84:85], v78 offset:8
	ds_read_b64 v[86:87], v78 offset:16
	ds_read_b64 v[88:89], v81
	ds_read_b64 v[90:91], v81 offset:8
	ds_read_b64 v[92:93], v81 offset:16
	v_add_u32_e32 v0, 0x1e800, v72
	ds_read_u16 v0, v0
	ds_read_b128 v[118:121], v77 offset:8192
	ds_read_b128 v[122:125], v77 offset:8704
	ds_read_b128 v[126:129], v77 offset:9216
	ds_read_b128 v[130:133], v77 offset:9728
	ds_read_b64 v[94:95], v80
	ds_read_b64 v[96:97], v80 offset:8
	ds_read_b64 v[98:99], v80 offset:16
	ds_read_b64 v[100:101], v79
	ds_read_b64 v[102:103], v79 offset:8
	ds_read_b64 v[104:105], v79 offset:16
	v_add_u32_e32 v1, 0x1ea00, v72
	ds_read_u16 v1, v1
	s_waitcnt vmcnt(0)
	s_waitcnt lgkmcnt(0)
	s_barrier
	s_setprio 1
	v_mov_b32_e32 v134, 0x7f7f7f7f
	s_waitcnt lgkmcnt(0)
	s_nop 0
	v_mfma_scale_f32_32x32x64_f8f6f4 v[50:65], v[82:87], v[66:69], v[50:65], v0, v134 op_sel_hi:[0,0,0] cbsz:2 blgp:4
	v_mfma_scale_f32_32x32x64_f8f6f4 v[34:49], v[82:87], v[106:109], v[34:49], v0, v134 op_sel_hi:[0,0,0] cbsz:2 blgp:4
	v_mfma_scale_f32_32x32x64_f8f6f4 v[18:33], v[82:87], v[110:113], v[18:33], v0, v134 op_sel_hi:[0,0,0] cbsz:2 blgp:4
	v_mfma_scale_f32_32x32x64_f8f6f4 v[2:17], v[82:87], v[114:117], v[2:17], v0, v134 op_sel_hi:[0,0,0] cbsz:2 blgp:4
	v_mfma_scale_f32_32x32x64_f8f6f4 v[50:65], v[88:93], v[66:69], v[50:65], v0, v134 op_sel:[1,0,0] op_sel_hi:[0,0,0] cbsz:2 blgp:4
	v_mfma_scale_f32_32x32x64_f8f6f4 v[34:49], v[88:93], v[106:109], v[34:49], v0, v134 op_sel:[1,0,0] op_sel_hi:[0,0,0] cbsz:2 blgp:4
	v_mfma_scale_f32_32x32x64_f8f6f4 v[18:33], v[88:93], v[110:113], v[18:33], v0, v134 op_sel:[1,0,0] op_sel_hi:[0,0,0] cbsz:2 blgp:4
	v_mfma_scale_f32_32x32x64_f8f6f4 v[2:17], v[88:93], v[114:117], v[2:17], v0, v134 op_sel:[1,0,0] op_sel_hi:[0,0,0] cbsz:2 blgp:4
	v_lshrrev_b32_e32 v0, 8, v1
	v_mfma_scale_f32_32x32x64_f8f6f4 v[50:65], v[94:99], v[118:121], v[50:65], v1, v134 op_sel_hi:[0,0,0] cbsz:2 blgp:4
	v_mfma_scale_f32_32x32x64_f8f6f4 v[34:49], v[94:99], v[122:125], v[34:49], v1, v134 op_sel_hi:[0,0,0] cbsz:2 blgp:4
	v_mfma_scale_f32_32x32x64_f8f6f4 v[18:33], v[94:99], v[126:129], v[18:33], v1, v134 op_sel_hi:[0,0,0] cbsz:2 blgp:4
	v_mfma_scale_f32_32x32x64_f8f6f4 v[2:17], v[94:99], v[130:133], v[2:17], v1, v134 op_sel_hi:[0,0,0] cbsz:2 blgp:4
	v_mfma_scale_f32_32x32x64_f8f6f4 v[50:65], v[100:105], v[118:121], v[50:65], v0, v134 op_sel_hi:[0,0,0] cbsz:2 blgp:4
	v_mfma_scale_f32_32x32x64_f8f6f4 v[34:49], v[100:105], v[122:125], v[34:49], v0, v134 op_sel_hi:[0,0,0] cbsz:2 blgp:4
	v_mfma_scale_f32_32x32x64_f8f6f4 v[18:33], v[100:105], v[126:129], v[18:33], v0, v134 op_sel_hi:[0,0,0] cbsz:2 blgp:4
	v_mfma_scale_f32_32x32x64_f8f6f4 v[2:17], v[100:105], v[130:133], v[2:17], v0, v134 op_sel_hi:[0,0,0] cbsz:2 blgp:4
	s_setprio 0
	s_barrier
	ds_read_b128 v[66:69], v77 offset:40960
	ds_read_b128 v[102:105], v77 offset:41472
	ds_read_b128 v[106:109], v77 offset:41984
	ds_read_b128 v[110:113], v77 offset:42496
	ds_read_b64 v[78:79], v75
	ds_read_b64 v[80:81], v75 offset:8
	ds_read_b64 v[82:83], v75 offset:16
	ds_read_b64 v[84:85], v76
	ds_read_b64 v[86:87], v76 offset:8
	ds_read_b64 v[88:89], v76 offset:16
	v_add_u32_e32 v0, 0x1ec00, v72
	ds_read_u16 v0, v0
	ds_read_b128 v[114:117], v77 offset:49152
	ds_read_b128 v[118:121], v77 offset:49664
	ds_read_b128 v[122:125], v77 offset:50176
	ds_read_b128 v[126:129], v77 offset:50688
	ds_read_b64 v[90:91], v74
	ds_read_b64 v[92:93], v74 offset:8
	ds_read_b64 v[94:95], v74 offset:16
	ds_read_b64 v[96:97], v73
	ds_read_b64 v[98:99], v73 offset:8
	ds_read_b64 v[100:101], v73 offset:16
	v_add_u32_e32 v1, 0x1ee00, v72
	ds_read_u16 v1, v1
	s_waitcnt vmcnt(0)
	s_waitcnt lgkmcnt(0)
	s_barrier
	s_setprio 1
	s_waitcnt lgkmcnt(0)
	v_mfma_scale_f32_32x32x64_f8f6f4 v[50:65], v[78:83], v[66:69], v[50:65], v0, v134 op_sel_hi:[0,0,0] cbsz:2 blgp:4
	v_mfma_scale_f32_32x32x64_f8f6f4 v[34:49], v[78:83], v[102:105], v[34:49], v0, v134 op_sel_hi:[0,0,0] cbsz:2 blgp:4
	v_mfma_scale_f32_32x32x64_f8f6f4 v[18:33], v[78:83], v[106:109], v[18:33], v0, v134 op_sel_hi:[0,0,0] cbsz:2 blgp:4
	v_mfma_scale_f32_32x32x64_f8f6f4 v[2:17], v[78:83], v[110:113], v[2:17], v0, v134 op_sel_hi:[0,0,0] cbsz:2 blgp:4
	v_mfma_scale_f32_32x32x64_f8f6f4 v[50:65], v[84:89], v[66:69], v[50:65], v0, v134 op_sel:[1,0,0] op_sel_hi:[0,0,0] cbsz:2 blgp:4
	v_mfma_scale_f32_32x32x64_f8f6f4 v[34:49], v[84:89], v[102:105], v[34:49], v0, v134 op_sel:[1,0,0] op_sel_hi:[0,0,0] cbsz:2 blgp:4
	v_mfma_scale_f32_32x32x64_f8f6f4 v[18:33], v[84:89], v[106:109], v[18:33], v0, v134 op_sel:[1,0,0] op_sel_hi:[0,0,0] cbsz:2 blgp:4
	v_mfma_scale_f32_32x32x64_f8f6f4 v[2:17], v[84:89], v[110:113], v[2:17], v0, v134 op_sel:[1,0,0] op_sel_hi:[0,0,0] cbsz:2 blgp:4
	v_lshrrev_b32_e32 v0, 8, v1
	v_mfma_scale_f32_32x32x64_f8f6f4 v[50:65], v[90:95], v[114:117], v[50:65], v1, v134 op_sel_hi:[0,0,0] cbsz:2 blgp:4
	v_mfma_scale_f32_32x32x64_f8f6f4 v[34:49], v[90:95], v[118:121], v[34:49], v1, v134 op_sel_hi:[0,0,0] cbsz:2 blgp:4
	v_mfma_scale_f32_32x32x64_f8f6f4 v[18:33], v[90:95], v[122:125], v[18:33], v1, v134 op_sel_hi:[0,0,0] cbsz:2 blgp:4
	v_mfma_scale_f32_32x32x64_f8f6f4 v[2:17], v[90:95], v[126:129], v[2:17], v1, v134 op_sel_hi:[0,0,0] cbsz:2 blgp:4
	v_mfma_scale_f32_32x32x64_f8f6f4 v[50:65], v[96:101], v[114:117], v[50:65], v0, v134 op_sel_hi:[0,0,0] cbsz:2 blgp:4
	v_mfma_scale_f32_32x32x64_f8f6f4 v[34:49], v[96:101], v[118:121], v[34:49], v0, v134 op_sel_hi:[0,0,0] cbsz:2 blgp:4
	v_mfma_scale_f32_32x32x64_f8f6f4 v[18:33], v[96:101], v[122:125], v[18:33], v0, v134 op_sel_hi:[0,0,0] cbsz:2 blgp:4
	v_mfma_scale_f32_32x32x64_f8f6f4 v[2:17], v[96:101], v[126:129], v[2:17], v0, v134 op_sel_hi:[0,0,0] cbsz:2 blgp:4
	s_setprio 0
	s_barrier
	s_cmpk_gt_u32 s33, 0xff
	s_cbranch_scc1 .LBB1_6
	s_barrier

	.amdhsa_kernel _Z9mxgemm_l3PKcS0_PKfPf
		.amdhsa_group_segment_fixed_size 0
		.amdhsa_private_segment_fixed_size 0
		.amdhsa_kernarg_size 32
		.amdhsa_user_sgpr_count 2
		.amdhsa_user_sgpr_dispatch_ptr 0
		.amdhsa_user_sgpr_queue_ptr 0
		.amdhsa_user_sgpr_kernarg_segment_ptr 1
		.amdhsa_user_sgpr_dispatch_id 0
		.amdhsa_user_sgpr_kernarg_preload_length 0
		.amdhsa_user_sgpr_kernarg_preload_offset 0
		.amdhsa_user_sgpr_private_segment_size 0
		.amdhsa_uses_dynamic_stack 0
		.amdhsa_enable_private_segment 0
		.amdhsa_system_sgpr_workgroup_id_x 1
		.amdhsa_system_sgpr_workgroup_id_y 0
		.amdhsa_system_sgpr_workgroup_id_z 0
		.amdhsa_system_sgpr_workgroup_info 0
		.amdhsa_system_vgpr_workitem_id 0
		.amdhsa_next_free_vgpr 176
		.amdhsa_next_free_sgpr 84
		.amdhsa_accum_offset 176
		.amdhsa_reserve_vcc 1
		.amdhsa_float_round_mode_32 0
		.amdhsa_float_round_mode_16_64 0
		.amdhsa_float_denorm_mode_32 3
		.amdhsa_float_denorm_mode_16_64 3
		.amdhsa_dx10_clamp 1
		.amdhsa_ieee_mode 1
		.amdhsa_fp16_overflow 0
		.amdhsa_tg_split 0
		.amdhsa_exception_fp_ieee_invalid_op 0
		.amdhsa_exception_fp_denorm_src 0
		.amdhsa_exception_fp_ieee_div_zero 0
		.amdhsa_exception_fp_ieee_overflow 0
		.amdhsa_exception_fp_ieee_underflow 0
		.amdhsa_exception_fp_ieee_inexact 0
		.amdhsa_exception_int_div_zero 0
	.end_amdhsa_kernel

amdhsa.kernels:
  - .agpr_count:     0
    .args:
      - .actual_access:  read_only
        .address_space:  global
        .offset:         0
        .size:           8
        .value_kind:     global_buffer
      - .actual_access:  read_only
        .address_space:  global
        .offset:         8
        .size:           8
        .value_kind:     global_buffer
      - .actual_access:  read_only
        .address_space:  global
        .offset:         16
        .size:           8
        .value_kind:     global_buffer
      - .actual_access:  read_only
        .address_space:  global
        .offset:         24
        .size:           8
        .value_kind:     global_buffer
      - .actual_access:  read_only
        .address_space:  global
        .offset:         32
        .size:           8
        .value_kind:     global_buffer
      - .actual_access:  read_only
        .address_space:  global
        .offset:         40
        .size:           8
        .value_kind:     global_buffer
      - .actual_access:  write_only
        .address_space:  global
        .offset:         48
        .size:           8
        .value_kind:     global_buffer
      - .actual_access:  write_only
        .address_space:  global
        .offset:         56
        .size:           8
        .value_kind:     global_buffer
      - .actual_access:  write_only
        .address_space:  global
        .offset:         64
        .size:           8
        .value_kind:     global_buffer
      - .actual_access:  write_only
        .address_space:  global
        .offset:         72
        .size:           8
        .value_kind:     global_buffer
      - .actual_access:  write_only
        .address_space:  global
        .offset:         80
        .size:           8
        .value_kind:     global_buffer
    .group_segment_fixed_size: 4608
    .kernarg_segment_align: 8
    .kernarg_segment_size: 88
    .language:       OpenCL C
    .language_version:
      - 2
      - 0
    .max_flat_workgroup_size: 256
    .name:           _Z8prep_allPKfS0_S0_S0_S0_S0_PcS1_S1_S1_S1_
    .private_segment_fixed_size: 0
    .sgpr_count:     18
    .sgpr_spill_count: 0
    .symbol:         _Z8prep_allPKfS0_S0_S0_S0_S0_PcS1_S1_S1_S1_.kd
    .uniform_work_group_size: 1
    .uses_dynamic_stack: false
    .vgpr_count:     61
    .vgpr_spill_count: 0
    .wavefront_size: 64
  - .agpr_count:     0
    .args:
      - .address_space:  global
        .offset:         0
        .size:           8
        .value_kind:     global_buffer
      - .address_space:  global
        .offset:         8
        .size:           8
        .value_kind:     global_buffer
      - .actual_access:  read_only
        .address_space:  global
        .offset:         16
        .size:           8
        .value_kind:     global_buffer
      - .actual_access:  write_only
        .address_space:  global
        .offset:         24
        .size:           8
        .value_kind:     global_buffer
    .group_segment_fixed_size: 0
    .kernarg_segment_align: 8
    .kernarg_segment_size: 32
    .language:       OpenCL C
    .language_version:
      - 2
      - 0
    .max_flat_workgroup_size: 512
    .name:           _Z9mxgemm_l3PKcS0_PKfPf
    .private_segment_fixed_size: 0
    .sgpr_count:     90
    .sgpr_spill_count: 0
    .symbol:         _Z9mxgemm_l3PKcS0_PKfPf.kd
    .uniform_work_group_size: 1
    .uses_dynamic_stack: false
    .vgpr_count:     176
    .vgpr_spill_count: 0
    .wavefront_size: 64
  - .agpr_count:     0
    .args:
      - .address_space:  global
        .offset:         0
        .size:           8
        .value_kind:     global_buffer
      - .address_space:  global
        .offset:         8
        .size:           8
        .value_kind:     global_buffer
      - .actual_access:  read_only
        .address_space:  global
        .offset:         16
        .size:           8
        .value_kind:     global_buffer
      - .actual_access:  read_only
        .address_space:  global
        .offset:         24
        .size:           8
        .value_kind:     global_buffer
      - .actual_access:  write_only
        .address_space:  global
        .offset:         32
        .size:           8
        .value_kind:     global_buffer
      - .offset:         40
        .size:           4
        .value_kind:     by_value
    .group_segment_fixed_size: 0
    .kernarg_segment_align: 8
    .kernarg_segment_size: 44
    .language:       OpenCL C
    .language_version:
      - 2
      - 0
    .max_flat_workgroup_size: 512
    .name:           _Z6mxgemmILi0ELi1024ELi4EEvPKcS1_PKfS3_Pvi
    .private_segment_fixed_size: 0
    .sgpr_count:     90
    .sgpr_spill_count: 0
    .symbol:         _Z6mxgemmILi0ELi1024ELi4EEvPKcS1_PKfS3_Pvi.kd
    .uniform_work_group_size: 1
    .uses_dynamic_stack: false
    .vgpr_count:     248
    .vgpr_spill_count: 0
    .wavefront_size: 64
  - .agpr_count:     0
    .args:
      - .address_space:  global
        .offset:         0
        .size:           8
        .value_kind:     global_buffer
      - .address_space:  global
        .offset:         8
        .size:           8
        .value_kind:     global_buffer
      - .actual_access:  read_only
        .address_space:  global
        .offset:         16
        .size:           8
        .value_kind:     global_buffer
      - .actual_access:  read_only
        .address_space:  global
        .offset:         24
        .size:           8
        .value_kind:     global_buffer
      - .actual_access:  write_only
        .address_space:  global
        .offset:         32
        .size:           8
        .value_kind:     global_buffer
      - .offset:         40
        .size:           4
        .value_kind:     by_value
    .group_segment_fixed_size: 0
    .kernarg_segment_align: 8
    .kernarg_segment_size: 44
    .language:       OpenCL C
    .language_version:
      - 2
      - 0
    .max_flat_workgroup_size: 512
    .name:           _Z6mxgemmILi1ELi4096ELi4EEvPKcS1_PKfS3_Pvi
    .private_segment_fixed_size: 0
    .sgpr_count:     90
    .sgpr_spill_count: 0
    .symbol:         _Z6mxgemmILi1ELi4096ELi4EEvPKcS1_PKfS3_Pvi.kd
    .uniform_work_group_size: 1
    .uses_dynamic_stack: false
    .vgpr_count:     256
    .vgpr_spill_count: 0
    .wavefront_size: 64
